# idle-slot filling in phases 3 and 5 (2 tiles per workgroup without a 5th RG-LRU item / ctx unit) on top of full layer-1 deferral, quotas 6/10/9/12
# baseline (speedup 1.0000x reference)
; #define SEAM(k) do { if (IN(k) && IN((k) + 1)) xcd_barrier(bar); \
;         if (PROBE_MASK) { const unsigned long long t_ = __builtin_amdgcn_s_memrealtime(); if ((PROBE_MASK >> (k)) & 1u) pr_acc += t_ - pr_t0; pr_t0 = t_; } } while (0)
; __device__ __forceinline__ void convert_deferred(const Ptrs& P, unsigned char* lds, int quota) {
;     const int tid = threadIdx.x, wid = tid >> 6, lane = tid & 63;
;     float* tile = (float*)lds;
;     volatile __attribute__((address_space(3))) int* slot = (volatile __attribute__((address_space(3))) int*)((__attribute__((address_space(3))) unsigned char*)lds + 131072 + 320 + 11000);
;     unsigned* q = (unsigned*)(P.ws + WS_CTL) + CW_DEFQ;
;     for (int n = 0; n < quota; ++n) {
;         __syncthreads();
;         if (tid == 0) *slot = (int)atomicAdd(q, 1u);
;         __syncthreads();
;         const int t = *slot;
;         if (t >= DEF_GU + DEF_DN) break;
; __global__ void __launch_bounds__(NT, 2) mega(Args args) {
;     ...
;     if (IN(3)) {
;         { g8::UpOrder S{(const char*)Z, (const char*)(ws + WS_WUQ), (const char*)(ws + WS_WUKV), G, (int)blockIdx.x}; g8::EpiStoreBf16 E{(bf16*)(ws + WS_QP), 1792};
;           g8::gemm_phase<g8::EpiStoreBf16, g8::UpOrder, false, true>(LDSP, EVEN_IN_P, 384, S, E); }
;         ph_lru(P, lds, 0, 0);
;     } SEAM(3);
.LBB0_903:
	s_waitcnt vmcnt(0)
	s_barrier
	s_cmp_lt_u32 s2, 64
	s_cbranch_scc1 .Lcd3_skip
	v_lshlrev_b32_e32 v250, 2, v0
	v_lshlrev_b32_e32 v251, 3, v0
	s_waitcnt vmcnt(0) lgkmcnt(0)
	v_and_b32_e32 v186, 0x7c, v250
	v_lshlrev_b32_e32 v187, 5, v0
	s_movk_i32 s0, 0x400
	v_and_or_b32 v196, v187, s0, v186
	v_lshrrev_b32_e32 v186, 3, v0
	v_and_b32_e32 v198, 56, v186
	v_lshrrev_b32_e32 v186, 3, v182
	v_lshl_or_b32 v188, v1, 5, v186
	v_lshl_add_u32 v189, v182, 4, 0
	v_and_b32_e32 v186, 56, v251
	v_lshl_add_u32 v191, v188, 2, 0
	v_mul_u32_u24_e32 v195, 0x2020, v1
	v_lshlrev_b32_e32 v188, 6, v188
	v_mul_u32_u24_e32 v193, 0x404, v186
	v_or_b32_e32 v190, 0x200, v188
	v_or_b32_e32 v192, 0x400, v188
	v_or_b32_e32 v194, 0x600, v188
	s_add_i32 s10, 0, 0x22c38
	v_add_u32_e32 v200, v189, v195
	v_and_b32_e32 v197, 0xfc, v250
	s_mov_b32 s1, 0
	v_mov_b32_e32 v187, 0
	s_mov_b32 s3, 2
	v_mov_b32_e32 v199, s10
	s_movk_i32 s11, 0x17ff
	s_movk_i32 s80, 0x800
	s_mov_b32 s81, 0x1104e000
	s_movk_i32 s14, -2048
	v_add_u32_e32 v201, 0x404, v200
	v_add_u32_e32 v202, 0x40c, v200
	v_add_u32_e32 v203, 0x808, v200
	v_add_u32_e32 v204, 0xc0c, v200
	v_add_u32_e32 v205, 0xc14, v200
	v_add_u32_e32 v206, 0x1414, v200
	v_add_u32_e32 v207, 0x141c, v200
	v_add_u32_e32 v208, 0x1818, v200
	v_add_u32_e32 v209, 0x1c1c, v200
	v_add_u32_e32 v210, 0x1c24, v200
	v_lshlrev_b32_e32 v186, 1, v186
	v_add_u32_e32 v211, v191, v193
	v_lshlrev_b32_e32 v188, 1, v188
	v_lshlrev_b32_e32 v190, 1, v190
	v_lshlrev_b32_e32 v192, 1, v192
	v_lshlrev_b32_e32 v194, 1, v194
	s_branch .Lcd3_2280

; __device__ __forceinline__ unsigned g8_cvt_pk(float lo, float hi) { unsigned r; asm volatile("v_cvt_pk_bf16_f32 %0, %1, %2" : "=v"(r) : "v"(lo), "v"(hi)); return r; }
; __device__ __forceinline__ void bt_load(const float* __restrict__ src, int N, int perm, int it, int ntn, f32x4 (&v)[8]) {
;     const int wid = threadIdx.x >> 6, lane = threadIdx.x & 63;
;     const int per = 16 * ntn, z = it / per, r = it % per, kt = r / ntn, nt = r % ntn;
;     const int np = nt * 256 + lane * 4;
;     const int sc = perm ? (nt * 128 + (lane & 31) * 4 + (lane >> 5) * 1024) : np;
;     const float* p = src + (size_t)z * 1024 * N + (size_t)(kt * 64 + wid * 8) * N + sc;
; #pragma unroll
;     for (int i = 0; i < 8; ++i) v[i] = __builtin_nontemporal_load((const f32x4*)(p + (size_t)i * N));
; }
; __device__ __forceinline__ void convert_deferred(const Ptrs& P, unsigned char* lds, int quota) {
;     ...
;         __syncthreads();
;         if (tid == 0) *slot = (int)atomicAdd(q, 1u);
;         __syncthreads();
;         const int t = *slot;
;         if (t >= DEF_GU + DEF_DN) break;
;         const bool gu = t < DEF_GU;
;         const float* src = gu ? P.in[34] : P.in[36]; bf16* dst = (bf16*)(P.ws + (gu ? WS_WGU : WS_WDN));
;         const int N = gu ? 2048 : 1024, ntn = N / 256, it = gu ? 2 * NE * 16 * 8 - DEF_GU + t : 2 * NE * 16 * 4 - DEF_DN + (t - DEF_GU);
;         f32x4 cur[8];
;         bt_load(src, N, gu ? 1 : 0, it, ntn, cur);
; #pragma unroll
;         for (int i = 0; i < 8; ++i) { float* tp = tile + (wid * 8 + i) * 257 + lane * 4; tp[0] = cur[i][0]; tp[1] = cur[i][1]; tp[2] = cur[i][2]; tp[3] = cur[i][3]; }
;         __syncthreads();
;         const int per = 16 * ntn, z = it / per, r = it % per, kt = r / ntn, nt = r % ntn;
;         bf16* d = dst + (size_t)z * N * 1024 + (((size_t)nt * 16 + kt) << 14);
;         const int kc = lane & 7;
; #pragma unroll
;         for (int pss = 0; pss < 4; ++pss) {
;             const int nn = wid * 32 + pss * 8 + (lane >> 3); float f[8];
; #pragma unroll
;             for (int j = 0; j < 8; ++j) f[j] = tile[(kc * 8 + j) * 257 + nn];
;             u32x4 w; w.x = g8_cvt_pk(f[0], f[1]); w.y = g8_cvt_pk(f[2], f[3]); w.z = g8_cvt_pk(f[4], f[5]); w.w = g8_cvt_pk(f[6], f[7]);
;             *(u32x4*)(d + nn * 64 + kc * 8) = w;
;         }
.Lcd3_2284:
	s_or_b64 exec, exec, s[4:5]
	s_waitcnt lgkmcnt(0)
	s_barrier
	ds_read_b32 v189, v199
	s_mov_b64 s[4:5], -1
	s_waitcnt lgkmcnt(0)
	v_cmp_lt_i32_e32 vcc, s11, v189
	v_readfirstlane_b32 s0, v189
	s_cbranch_vccnz .Lcd3_2279
	s_cmpk_gt_i32 s0, 0xfff
	s_cselect_b64 vcc, -1, 0
	s_and_b64 s[4:5], vcc, exec
	s_cselect_b32 s4, s81, 0x104e000
	s_cselect_b32 s9, 0x400, s80
	s_cselect_b32 s15, s73, s69
	s_cselect_b32 s84, s72, s68
	s_cselect_b32 s5, s14, 0x1000
	s_cselect_b32 s82, 20, 21
	s_cselect_b32 s85, 10, 11
	s_add_u32 s86, s78, s4
	s_addc_u32 s87, s79, 0
	s_lshr_b32 s6, s9, 4
	s_abs_i32 s4, s6
	v_cvt_f32_u32_e32 v189, s4
	s_sub_i32 s83, 0, s4
	s_add_i32 s5, s5, s0
	s_abs_i32 s7, s5
	v_rcp_iflag_f32_e32 v189, v189
	s_xor_b32 s0, s5, s6
	s_lshr_b32 s8, s9, 8
	s_ashr_i32 s0, s0, 31
	v_mul_f32_e32 v189, 0x4f7ffffe, v189
	v_cvt_u32_f32_e32 v189, v189
	s_nop 0
	v_readfirstlane_b32 s88, v189
	s_mul_i32 s83, s83, s88
	s_mul_hi_u32 s83, s88, s83
	s_add_i32 s88, s88, s83
	s_mul_hi_u32 s83, s7, s88
	s_mul_i32 s88, s83, s4
	s_sub_i32 s7, s7, s88
	s_add_i32 s88, s83, 1
	s_sub_i32 s89, s7, s4
	s_cmp_ge_u32 s7, s4
	s_cselect_b32 s83, s88, s83
	s_cselect_b32 s7, s89, s7
	s_add_i32 s88, s83, 1
	s_cmp_ge_u32 s7, s4
	s_cselect_b32 s4, s88, s83
	s_xor_b32 s4, s4, s0
	s_sub_i32 s4, s4, s0
	s_sext_i32_i8 s0, s8
	v_cvt_f32_i32_e32 v189, s0
	s_mul_i32 s6, s4, s6
	s_sub_i32 s5, s5, s6
	v_cvt_f32_i32_e32 v191, s5
	v_rcp_iflag_f32_e32 v193, v189
	s_xor_b32 s0, s5, s0
	s_ashr_i32 s0, s0, 30
	s_or_b32 s0, s0, 1
	v_mul_f32_e32 v193, v191, v193
	v_trunc_f32_e32 v193, v193
	v_fma_f32 v191, -v193, v189, v191
	v_cvt_i32_f32_e32 v193, v193
	v_cmp_ge_f32_e64 s[6:7], |v191|, |v189|
	s_and_b64 s[6:7], s[6:7], exec
	s_cselect_b32 s0, s0, 0
	v_readfirstlane_b32 s6, v193
	s_add_i32 s6, s6, s0
	s_mul_i32 s7, s6, s8
	s_sub_i32 s8, s5, s7
	s_sext_i32_i8 s5, s8
	v_lshl_add_u32 v189, s5, 7, v196
	v_lshl_or_b32 v191, s5, 8, v197
	s_ashr_i32 s5, s4, 31
	s_sext_i32_i8 s0, s6
	s_lshl_b64 s[82:83], s[4:5], s82
	v_lshl_or_b32 v214, s0, 6, v198
	s_lshl_b64 s[82:83], s[82:83], 2
	v_ashrrev_i32_e32 v215, 31, v214
	s_add_u32 s82, s84, s82
	v_cndmask_b32_e32 v212, v189, v191, vcc
	s_addc_u32 s83, s15, s83
	v_lshlrev_b64 v[214:215], s85, v[214:215]
	v_lshl_add_u64 v[214:215], v[214:215], 2, s[82:83]
	v_ashrrev_i32_e32 v213, 31, v212
	v_lshl_add_u64 v[236:237], v[212:213], 2, v[214:215]
	s_lshl_b32 s0, s9, 2
	s_lshl_b64 s[82:83], 12, s85
	v_lshl_add_u64 v[220:221], v[236:237], 0, s[0:1]
	v_lshl_add_u64 v[228:229], v[236:237], 0, s[82:83]
	s_lshl_b64 s[82:83], 24, s85
	v_lshl_add_u64 v[238:239], v[220:221], 0, s[0:1]
	v_lshl_add_u64 v[240:241], v[236:237], 0, s[82:83]
	s_lshl_b64 s[82:83], 28, s85
	s_lshl_b32 s0, s9, 3
	v_lshl_add_u64 v[242:243], v[236:237], 0, s[82:83]
	v_lshl_add_u64 v[244:245], v[238:239], 0, s[0:1]
	s_lshl_b64 s[82:83], 20, s85
	global_load_dwordx4 v[212:215], v[236:237], off nt
	global_load_dwordx4 v[216:219], v[220:221], off nt
	s_nop 0
	global_load_dwordx4 v[220:223], v[238:239], off nt
	global_load_dwordx4 v[224:227], v[228:229], off nt
	s_nop 0
	global_load_dwordx4 v[228:231], v[240:241], off nt
	global_load_dwordx4 v[232:235], v[242:243], off nt
	v_lshl_add_u64 v[246:247], v[236:237], 0, s[82:83]
	global_load_dwordx4 v[236:239], v[244:245], off nt
	global_load_dwordx4 v[240:243], v[246:247], off nt
	s_lshl_b64 s[4:5], s[4:5], s85
	s_lshl_b64 s[4:5], s[4:5], 11
	s_add_u32 s0, s86, s4
	s_addc_u32 s9, s87, s5
	s_bfe_i64 s[4:5], s[8:9], 0x80000
	s_bfe_i64 s[6:7], s[6:7], 0x80000
	s_lshl_b64 s[4:5], s[4:5], 19
	s_add_u32 s0, s0, s4
	s_addc_u32 s8, s9, s5
	s_lshl_b64 s[4:5], s[6:7], 15
	s_add_u32 s4, s0, s4
	s_addc_u32 s5, s8, s5
	v_mov_b32_e32 v189, v187
	s_add_i32 s3, s3, -1
	s_cmp_eq_u32 s3, 0
	s_waitcnt vmcnt(7)
	ds_write_b128 v200, v[212:215]
	s_waitcnt vmcnt(6)
	ds_write2_b32 v201, v216, v217 offset1:1
	ds_write2_b32 v202, v218, v219 offset1:1
	s_waitcnt vmcnt(3)
	ds_write2_b64 v208, v[228:229], v[230:231] offset1:1
	s_waitcnt vmcnt(2)
	ds_write2_b32 v209, v232, v233 offset1:1
	ds_write2_b32 v210, v234, v235 offset1:1
	ds_write2_b64 v203, v[220:221], v[222:223] offset1:1
	ds_write2_b32 v204, v224, v225 offset1:1
	ds_write2_b32 v205, v226, v227 offset1:1
	s_waitcnt vmcnt(1)
	ds_write_b128 v200, v[236:239] offset:4112
	s_waitcnt vmcnt(0)
	ds_write2_b32 v206, v240, v241 offset1:1
	ds_write2_b32 v207, v242, v243 offset1:1
	s_waitcnt lgkmcnt(0)
	s_barrier
	ds_read_b32 v191, v211 offset:1028
	ds_read_b32 v193, v211 offset:3084
	ds_read_b32 v195, v211 offset:5140
	ds_read_b32 v215, v211 offset:7196
	ds_read_b32 v216, v211 offset:6168
	ds_read_b32 v214, v211 offset:4112
	ds_read_b32 v213, v211 offset:2056
	ds_read_b32 v212, v211
	s_waitcnt lgkmcnt(0)
	v_cvt_pk_bf16_f32 v212, v212, v191
	v_cvt_pk_bf16_f32 v213, v213, v193
	v_cvt_pk_bf16_f32 v214, v214, v195
	v_cvt_pk_bf16_f32 v215, v216, v215
	ds_read_b32 v191, v211 offset:1060
	ds_read_b32 v193, v211 offset:3116
	ds_read_b32 v195, v211 offset:5172
	ds_read_b32 v220, v211 offset:7228
	ds_read_b32 v221, v211 offset:6200
	ds_read_b32 v222, v211 offset:4144
	ds_read_b32 v223, v211 offset:2088
	ds_read_b32 v224, v211 offset:32
	v_lshl_add_u64 v[216:217], s[4:5], 0, v[186:187]
	v_lshl_add_u64 v[218:219], v[216:217], 0, v[188:189]
	global_store_dwordx4 v[218:219], v[212:215], off
	s_cselect_b64 s[4:5], -1, 0
	s_waitcnt lgkmcnt(0)
	v_cvt_pk_bf16_f32 v212, v224, v191
	v_cvt_pk_bf16_f32 v213, v223, v193
	v_cvt_pk_bf16_f32 v214, v222, v195
	v_cvt_pk_bf16_f32 v215, v221, v220
	ds_read_b32 v189, v211 offset:1092
	ds_read_b32 v193, v211 offset:3148
	ds_read_b32 v195, v211 offset:5204
	ds_read_b32 v220, v211 offset:6232
	ds_read_b32 v221, v211 offset:4176
	ds_read_b32 v222, v211 offset:2120
	ds_read_b32 v223, v211 offset:64
	ds_read_b32 v224, v211 offset:7260
	v_mov_b32_e32 v191, v187
	v_lshl_add_u64 v[218:219], v[216:217], 0, v[190:191]
	global_store_dwordx4 v[218:219], v[212:215], off
	s_waitcnt lgkmcnt(1)
	s_nop 0
	v_cvt_pk_bf16_f32 v212, v223, v189
	v_cvt_pk_bf16_f32 v213, v222, v193
	v_cvt_pk_bf16_f32 v214, v221, v195
	s_waitcnt lgkmcnt(0)
	v_cvt_pk_bf16_f32 v215, v220, v224
	ds_read_b32 v189, v211 offset:1124
	ds_read_b32 v191, v211 offset:3180
	ds_read_b32 v195, v211 offset:5236
	ds_read_b32 v220, v211 offset:6264
	ds_read_b32 v221, v211 offset:4208
	ds_read_b32 v222, v211 offset:2152
	ds_read_b32 v223, v211 offset:96
	ds_read_b32 v224, v211 offset:7292
	v_mov_b32_e32 v193, v187
	v_lshl_add_u64 v[218:219], v[216:217], 0, v[192:193]
	global_store_dwordx4 v[218:219], v[212:215], off
	s_waitcnt lgkmcnt(1)
	s_nop 0
	v_cvt_pk_bf16_f32 v212, v223, v189
	v_cvt_pk_bf16_f32 v213, v222, v191
	v_cvt_pk_bf16_f32 v214, v221, v195
	v_mov_b32_e32 v195, v187
	v_lshl_add_u64 v[216:217], v[216:217], 0, v[194:195]
	s_waitcnt lgkmcnt(0)
	v_cvt_pk_bf16_f32 v215, v220, v224
	global_store_dwordx4 v[216:217], v[212:215], off
	s_branch .Lcd3_2279

; #define SEAM(k) do { if (IN(k) && IN((k) + 1)) xcd_barrier(bar); \
;         if (PROBE_MASK) { const unsigned long long t_ = __builtin_amdgcn_s_memrealtime(); if ((PROBE_MASK >> (k)) & 1u) pr_acc += t_ - pr_t0; pr_t0 = t_; } } while (0)
; __device__ __forceinline__ void convert_deferred(const Ptrs& P, unsigned char* lds, int quota) {
;     const int tid = threadIdx.x, wid = tid >> 6, lane = tid & 63;
;     float* tile = (float*)lds;
;     volatile __attribute__((address_space(3))) int* slot = (volatile __attribute__((address_space(3))) int*)((__attribute__((address_space(3))) unsigned char*)lds + 131072 + 320 + 11000);
;     unsigned* q = (unsigned*)(P.ws + WS_CTL) + CW_DEFQ;
;     for (int n = 0; n < quota; ++n) {
;         __syncthreads();
;         if (tid == 0) *slot = (int)atomicAdd(q, 1u);
;         __syncthreads();
;         const int t = *slot;
;         if (t >= DEF_GU + DEF_DN) break;
; __global__ void __launch_bounds__(NT, 2) mega(Args args) {
;     ...
;     if (IN(5)) {
;         ph_lru(P, lds, 1, 128);
;         for (int it = vcu; it < 256 + 16; it += G) {
;             if (it < 256) mla_attn_unit(P, lds, it / 64, (it / 16) % 4, it % 16, 0, sub_acc);
;             else { const int i2 = it - 256; mla_attn_unit(P, lds, i2 / 4, i2 % 4, 0, 1, sub_acc); }
;         }
;         prefetch_resid(P, 0, LDSP);
;     } SEAM(5);
.LBB0_1211:
	s_and_b32 s0, s2, 7
	s_cmp_lt_u32 s2, 128
	s_cbranch_scc0 .Lcd5_hi
	s_cmp_eq_u32 s0, 0
	s_cbranch_scc1 .Lcd5_skip
	s_branch .Lcd5_go
.Lcd5_hi:
	s_cmp_lt_u32 s2, 192
	s_cbranch_scc1 .Lcd5_skip
.Lcd5_go:
	v_lshlrev_b32_e32 v250, 2, v0
	v_lshlrev_b32_e32 v251, 3, v0
	s_waitcnt vmcnt(0) lgkmcnt(0)
	v_and_b32_e32 v186, 0x7c, v250
	v_lshlrev_b32_e32 v187, 5, v0
	s_movk_i32 s0, 0x400
	v_and_or_b32 v196, v187, s0, v186
	v_lshrrev_b32_e32 v186, 3, v0
	v_and_b32_e32 v198, 56, v186
	v_lshrrev_b32_e32 v186, 3, v182
	v_lshl_or_b32 v188, v1, 5, v186
	v_lshl_add_u32 v189, v182, 4, 0
	v_and_b32_e32 v186, 56, v251
	v_lshl_add_u32 v191, v188, 2, 0
	v_mul_u32_u24_e32 v195, 0x2020, v1
	v_lshlrev_b32_e32 v188, 6, v188
	v_mul_u32_u24_e32 v193, 0x404, v186
	v_or_b32_e32 v190, 0x200, v188
	v_or_b32_e32 v192, 0x400, v188
	v_or_b32_e32 v194, 0x600, v188
	s_add_i32 s10, 0, 0x22c38
	v_add_u32_e32 v200, v189, v195
	v_and_b32_e32 v197, 0xfc, v250
	s_mov_b32 s1, 0
	v_mov_b32_e32 v187, 0
	s_mov_b32 s3, 2
	v_mov_b32_e32 v199, s10
	s_movk_i32 s11, 0x17ff
	s_movk_i32 s80, 0x800
	s_mov_b32 s81, 0x1104e000
	s_movk_i32 s14, -2048
	v_add_u32_e32 v201, 0x404, v200
	v_add_u32_e32 v202, 0x40c, v200
	v_add_u32_e32 v203, 0x808, v200
	v_add_u32_e32 v204, 0xc0c, v200
	v_add_u32_e32 v205, 0xc14, v200
	v_add_u32_e32 v206, 0x1414, v200
	v_add_u32_e32 v207, 0x141c, v200
	v_add_u32_e32 v208, 0x1818, v200
	v_add_u32_e32 v209, 0x1c1c, v200
	v_add_u32_e32 v210, 0x1c24, v200
	v_lshlrev_b32_e32 v186, 1, v186
	v_add_u32_e32 v211, v191, v193
	v_lshlrev_b32_e32 v188, 1, v188
	v_lshlrev_b32_e32 v190, 1, v190
	v_lshlrev_b32_e32 v192, 1, v192
	v_lshlrev_b32_e32 v194, 1, v194
	s_branch .Lcd5_2280

; __device__ __forceinline__ unsigned xb_add(unsigned* p, unsigned v) { return __hip_atomic_fetch_add(p, v, __ATOMIC_RELAXED, __HIP_MEMORY_SCOPE_AGENT); }
; __device__ __forceinline__ void xcd_barrier(const XcdBarrier& b) {
;     asm volatile("s_waitcnt vmcnt(0)" ::: "memory");
;     __syncthreads();
;     if (threadIdx.x == 0) {
;         unsigned* bar = b.bar;
;         __builtin_amdgcn_s_waitcnt(0);
;         unsigned nloc = b.st[0], nx = b.st[1];
;         if (nloc == 0u) { xcd_barrier_complete(bar, b.x, nloc, nx); b.st[0] = nloc; b.st[1] = nx; }
;         const unsigned old = xb_add(&bar[XB_XSUB(b.x)], 1u);
; __device__ __forceinline__ void convert_deferred(const Ptrs& P, unsigned char* lds, int quota) {
;     ...
;     __syncthreads();
.Lcd5_2286:
	s_barrier
.Lcd5_skip:
	s_cmp_gt_i32 s97, 6
	s_cselect_b64 s[0:1], -1, 0
	s_and_b64 s[4:5], s[34:35], s[0:1]
	s_andn2_b64 vcc, exec, s[4:5]
	s_cbranch_vccnz .LBB0_1265
	s_waitcnt vmcnt(0)
	s_waitcnt vmcnt(0) lgkmcnt(0)
	s_barrier
	s_mov_b64 s[4:5], exec
	v_readlane_b32 s6, v254, 22
	v_readlane_b32 s7, v254, 23
	s_and_b64 s[6:7], s[4:5], s[6:7]
	s_mov_b64 exec, s[6:7]
	s_cbranch_execz .LBB0_1264
	s_add_i32 s3, 0, 0x20160
	v_mov_b32_e32 v2, s3
	s_waitcnt vmcnt(0) expcnt(0) lgkmcnt(0)
	ds_read_b32 v4, v2
	s_add_i32 s3, 0, 0x20164
	v_mov_b32_e32 v2, s3
	ds_read_b32 v2, v2
	s_waitcnt lgkmcnt(1)
	v_cmp_ne_u32_e32 vcc, 0, v4
	s_cbranch_vccnz .LBB0_1228
	v_readlane_b32 s6, v254, 0
	v_readlane_b32 s7, v254, 1
	s_load_dwordx2 s[10:11], s[6:7], 0x4
	s_add_u32 s6, s78, 0x4200
	s_addc_u32 s7, s79, 0
	s_add_u32 s8, s78, 0x4400
	s_addc_u32 s9, s79, 0
	s_waitcnt lgkmcnt(0)
	s_mul_i32 s3, s10, s62
	s_add_u32 s10, s78, 0x4500
	s_mul_i32 s3, s3, s11
	s_addc_u32 s11, s79, 0
	s_add_u32 s12, s78, 0x4600
	s_addc_u32 s13, s79, 0
	s_add_u32 s14, s78, 0x4700
	s_addc_u32 s15, s79, 0
	s_add_u32 s16, s78, 0x4800
	s_addc_u32 s17, s79, 0
	s_add_u32 s18, s78, 0x4900
	s_addc_u32 s19, s79, 0
	s_add_u32 s20, s78, 0x4a00
	s_addc_u32 s21, s79, 0
	s_add_u32 s22, s78, 0x4b00
	s_addc_u32 s23, s79, 0
	s_add_u32 s24, s78, 0x4c00
	s_addc_u32 s25, s79, 0
	s_add_u32 s26, s78, 0x4d00
	s_addc_u32 s27, s79, 0
	s_add_u32 s28, s78, 0x4e00
	s_addc_u32 s29, s79, 0
	s_add_u32 s30, s78, 0x4f00
	s_addc_u32 s31, s79, 0
	s_add_u32 s34, s78, 0x5000
	s_addc_u32 s35, s79, 0
	s_add_u32 s36, s78, 0x5100
	s_addc_u32 s37, s79, 0
	s_add_u32 s38, s78, 0x5200
	s_addc_u32 s39, s79, 0
	s_add_u32 s40, s78, 0x5300
	s_addc_u32 s41, s79, 0
	s_mov_b32 s33, 1
	v_mov_b32_e32 v18, 0
	s_branch .LBB0_1216
